# P5b: DPP lane-pair exchange so every store writes a full 32-B sector; grid barrier: XCD-last arrivers count directly on the generation word (one atomic round trip less)
# speedup vs baseline: 1.0246x; 1.0114x over previous
.LBB0_157:
	s_or_b64 exec, exec, s[4:5]
	v_cvt_f32_u32_e32 v4, v2
	s_waitcnt vmcnt(0)
	v_readfirstlane_b32 s3, v3
	v_sub_u32_e32 v3, 0, v2
	v_rcp_iflag_f32_e32 v4, v4
	v_add_u32_e32 v5, s3, v1
	v_mul_f32_e32 v4, 0x4f7ffffe, v4
	v_cvt_u32_f32_e32 v4, v4
	v_mul_lo_u32 v1, v3, v4
	v_mul_hi_u32 v1, v4, v1
	v_add_u32_e32 v1, v4, v1
	v_mul_hi_u32 v1, v5, v1
	v_mul_lo_u32 v3, v1, v2
	v_sub_u32_e32 v3, v5, v3
	v_add_u32_e32 v4, 1, v1
	v_cmp_ge_u32_e32 vcc, v3, v2
	s_nop 1
	v_cndmask_b32_e32 v1, v1, v4, vcc
	v_sub_u32_e32 v4, v3, v2
	v_cndmask_b32_e32 v3, v3, v4, vcc
	v_add_u32_e32 v4, 1, v1
	v_cmp_ge_u32_e32 vcc, v3, v2
	v_add_u32_e32 v3, 1, v5
	s_nop 0
	v_cndmask_b32_e32 v1, v1, v4, vcc
	v_mul_lo_u32 v4, v2, v1
	v_add_u32_e32 v2, v4, v2
	v_add_u32_e32 v252, 1, v1
	v_mul_lo_u32 v252, v252, v0
	v_cmp_ne_u32_e32 vcc, v3, v2
	s_cbranch_vccnz .Lxb_nl_0
	buffer_wbl2 sc1
	s_waitcnt vmcnt(0) lgkmcnt(0)
	v_mov_b32_e32 v253, 0x3500
	v_mov_b32_e32 v254, 1
	global_atomic_add v253, v254, s[56:57]
	s_mov_b64 vcc, exec
.Lxb_nl_0:
	s_and_saveexec_b64 s[4:5], vcc
	s_xor_b64 s[4:5], exec, s[4:5]
	s_cbranch_execz .LBB0_171
	s_waitcnt lgkmcnt(0)
	v_cmp_eq_u32_e32 vcc, v5, v4
	s_cbranch_vccz .Lxb_nf_0
	buffer_wbl2 sc1
.Lxb_nf_0:
	v_mov_b32_e32 v0, 0x3000
	global_load_dword v0, v0, s[56:57] offset:1280 sc1
	s_add_u32 s8, s56, 0x3500
	s_addc_u32 s9, s57, 0
	s_waitcnt vmcnt(0)
	v_cmp_lt_u32_e32 vcc, v0, v252
	s_and_saveexec_b64 s[6:7], vcc
	s_cbranch_execz .LBB0_170
	s_mov_b32 s3, 1
	s_mov_b64 s[10:11], 0
	v_mov_b32_e32 v0, 0
	s_branch .LBB0_161

.LBB0_165:
	global_load_dword v2, v0, s[8:9] sc1
	s_add_i32 s3, s3, 1
	s_mov_b64 s[16:17], -1
	s_waitcnt vmcnt(0)
	v_cmp_ge_u32_e32 vcc, v2, v252
	s_orn2_b64 s[14:15], vcc, exec
	s_branch .LBB0_160

.LBB0_171:
	s_andn2_saveexec_b64 s[4:5], s[4:5]
	s_cbranch_execz .LBB0_189
.LBB0_189:
	s_or_b64 exec, exec, s[0:1]
	s_waitcnt lgkmcnt(0)
	s_barrier

.LBB0_298:
	s_andn2_saveexec_b64 s[4:5], s[4:5]
	s_cbranch_execz .LBB0_316
.LBB0_316:
	s_or_b64 exec, exec, s[0:1]
	s_waitcnt lgkmcnt(0)
	s_barrier

.LBB0_448:
	s_andn2_saveexec_b64 s[4:5], s[4:5]
	s_cbranch_execz .LBB0_466
.LBB0_466:
	s_or_b64 exec, exec, s[0:1]
	s_waitcnt lgkmcnt(0)
	s_barrier

.LBB0_544:
	s_andn2_saveexec_b64 s[4:5], s[4:5]
	s_cbranch_execz .LBB0_562
.LBB0_562:
	s_or_b64 exec, exec, s[0:1]
	s_waitcnt lgkmcnt(0)
	s_barrier

.LBB0_701:
	s_andn2_saveexec_b64 s[4:5], s[4:5]
	s_cbranch_execz .LBB0_719
.LBB0_719:
	s_or_b64 exec, exec, s[0:1]
	s_waitcnt lgkmcnt(0)
	s_barrier

.LBB0_782:
	s_or_b64 exec, exec, s[8:9]
	v_cvt_f32_u32_e32 v4, v2
	s_waitcnt vmcnt(0)
	v_readfirstlane_b32 s8, v3
	v_sub_u32_e32 v3, 0, v2
	v_rcp_iflag_f32_e32 v4, v4
	v_add_u32_e32 v5, s8, v1
	v_mul_f32_e32 v4, 0x4f7ffffe, v4
	v_cvt_u32_f32_e32 v4, v4
	v_mul_lo_u32 v1, v3, v4
	v_mul_hi_u32 v1, v4, v1
	v_add_u32_e32 v1, v4, v1
	v_mul_hi_u32 v1, v5, v1
	v_mul_lo_u32 v3, v1, v2
	v_sub_u32_e32 v3, v5, v3
	v_add_u32_e32 v4, 1, v1
	v_cmp_ge_u32_e32 vcc, v3, v2
	s_nop 1
	v_cndmask_b32_e32 v1, v1, v4, vcc
	v_sub_u32_e32 v4, v3, v2
	v_cndmask_b32_e32 v3, v3, v4, vcc
	v_add_u32_e32 v4, 1, v1
	v_cmp_ge_u32_e32 vcc, v3, v2
	v_add_u32_e32 v3, 1, v5
	s_nop 0
	v_cndmask_b32_e32 v1, v1, v4, vcc
	v_mul_lo_u32 v4, v2, v1
	v_add_u32_e32 v2, v4, v2
	v_add_u32_e32 v252, 1, v1
	v_mul_lo_u32 v252, v252, v0
	v_cmp_ne_u32_e32 vcc, v3, v2
	s_cbranch_vccnz .Lxb_nl_5
	buffer_wbl2 sc1
	s_waitcnt vmcnt(0) lgkmcnt(0)
	v_mov_b32_e32 v253, 0x3500
	v_mov_b32_e32 v254, 1
	global_atomic_add v253, v254, s[56:57]
	s_mov_b64 vcc, exec
.Lxb_nl_5:
	s_and_saveexec_b64 s[8:9], vcc
	s_xor_b64 s[8:9], exec, s[8:9]
	s_cbranch_execz .LBB0_796
	s_waitcnt lgkmcnt(0)
	v_cmp_eq_u32_e32 vcc, v5, v4
	s_cbranch_vccz .Lxb_nf_5
	buffer_wbl2 sc1
.Lxb_nf_5:
	v_mov_b32_e32 v0, 0x3000
	global_load_dword v0, v0, s[56:57] offset:1280 sc1
	s_add_u32 s12, s56, 0x3500
	s_addc_u32 s13, s57, 0
	s_waitcnt vmcnt(0)
	v_cmp_lt_u32_e32 vcc, v0, v252
	s_and_saveexec_b64 s[10:11], vcc
	s_cbranch_execz .LBB0_795
	s_mov_b32 s33, 1
	s_mov_b64 s[14:15], 0
	v_mov_b32_e32 v0, 0
	s_branch .LBB0_786

.LBB0_790:
	global_load_dword v2, v0, s[12:13] sc1
	s_add_i32 s33, s33, 1
	s_mov_b64 s[38:39], -1
	s_waitcnt vmcnt(0)
	v_cmp_ge_u32_e32 vcc, v2, v252
	s_orn2_b64 s[36:37], vcc, exec
	s_branch .LBB0_785

.LBB0_796:
	s_andn2_saveexec_b64 s[8:9], s[8:9]
	s_cbranch_execz .LBB0_814
.LBB0_814:
	s_or_b64 exec, exec, s[0:1]
	s_waitcnt lgkmcnt(0)
	s_barrier
	s_nop 0
	v_add_u32_e32 v145, s44, v144
	v_cmp_gt_i32_e32 vcc, 64, v145
	s_and_saveexec_b64 s[0:1], vcc
	s_cbranch_execz .LBB0_816
	v_cvt_f32_i32_e32 v0, v145
	s_mov_b32 s8, 0x7f800000
	v_mov_b32_e32 v5, 0xbf1f24be
	v_mul_f32_e32 v0, 0x3d000000, v0
	v_mul_f32_e64 v2, |v0|, 0.5
	v_fract_f32_e32 v3, v2
	v_add_f32_e32 v3, v3, v3
	v_cmp_neq_f32_e32 vcc, s8, v2
	v_cmp_gt_f32_e64 s[8:9], |v0|, 1.0
	v_and_b32_e32 v1, 0x7fffffff, v0
	v_cndmask_b32_e32 v2, 0, v3, vcc
	v_cndmask_b32_e64 v2, |v0|, v2, s[8:9]
	v_add_f32_e32 v3, v2, v2
	v_rndne_f32_e32 v3, v3
	v_fmac_f32_e32 v2, -0.5, v3
	v_mul_f32_e32 v4, v2, v2
	v_fmac_f32_e32 v5, 0x3e75aa41, v4
	v_fmaak_f32 v5, v4, v5, 0x40234736
	v_fmaak_f32 v5, v4, v5, 0xc0a55e0e
	v_mul_f32_e32 v6, v2, v4
	v_mul_f32_e32 v5, v6, v5
	v_fmamk_f32 v2, v2, 0x40490fdb, v5
	v_mov_b32_e32 v5, 0x3e642e9d
	v_cvt_i32_f32_e32 v3, v3
	v_fmac_f32_e32 v5, 0x3d4be544, v4
	v_fmaak_f32 v5, v4, v5, 0xbfaad1da
	v_fmaak_f32 v5, v4, v5, 0x4081e0d3
	v_fmaak_f32 v5, v4, v5, 0xc09de9e6
	v_fma_f32 v4, v4, v5, 1.0
	v_lshlrev_b32_e32 v5, 30, v3
	v_and_b32_e32 v3, 1, v3
	v_cmp_eq_u32_e32 vcc, 0, v3
	s_brev_b32 s8, 1
	v_xor_b32_e32 v1, v1, v0
	v_cndmask_b32_e32 v3, v4, v2, vcc
	v_xor_b32_e32 v2, 0x80000000, v2
	v_cndmask_b32_e32 v2, v2, v4, vcc
	v_bitop3_b32 v2, v2, v5, s8 bitop3:0x78
	s_movk_i32 s8, 0x1f8
	v_and_b32_e32 v6, 0x80000000, v5
	v_xor_b32_e32 v1, v1, v3
	v_mov_b32_e32 v3, 0x7fc00000
	v_cmp_class_f32_e64 vcc, v0, s8
	v_xor_b32_e32 v1, v1, v6
	s_nop 0
	v_cndmask_b32_e32 v0, v3, v2, vcc
	v_lshl_add_u32 v2, v145, 2, 0
	v_cndmask_b32_e32 v1, v3, v1, vcc
	v_add_u32_e32 v2, 0x18000, v2
	ds_write2st64_b32 v2, v0, v1 offset1:1

.LBB0_821:
	s_lshl_b32 s0, s5, 6
	s_add_i32 s0, s0, s8
	v_lshlrev_b32_e32 v130, 3, v144
	s_ashr_i32 s1, s0, 31
	v_add_u32_e32 v128, 0xe00, v145
	v_and_b32_e32 v170, 0xf8, v130
	v_add_u32_e32 v130, 0xc00, v145
	v_add_u32_e32 v136, 0xa00, v145
	v_add_u32_e32 v138, 0x800, v145
	v_add_u32_e32 v148, 0x600, v145
	v_add_u32_e32 v150, 0x400, v145
	v_add_u32_e32 v156, 0x200, v145
	s_lshl_b64 s[0:1], s[0:1], 19
	v_ashrrev_i32_e32 v168, 5, v128
	v_ashrrev_i32_e32 v196, 5, v130
	v_ashrrev_i32_e32 v198, 5, v136
	v_ashrrev_i32_e32 v200, 5, v138
	v_ashrrev_i32_e32 v202, 5, v148
	v_ashrrev_i32_e32 v204, 5, v150
	v_ashrrev_i32_e32 v206, 5, v156
	v_ashrrev_i32_e32 v208, 5, v145
	s_add_u32 s0, s3, s0
	v_ashrrev_i32_e32 v169, 31, v168
	v_ashrrev_i32_e32 v197, 31, v196
	v_ashrrev_i32_e32 v199, 31, v198
	v_ashrrev_i32_e32 v201, 31, v200
	v_ashrrev_i32_e32 v203, 31, v202
	v_ashrrev_i32_e32 v205, 31, v204
	v_ashrrev_i32_e32 v207, 31, v206
	v_ashrrev_i32_e32 v209, 31, v208
	s_addc_u32 s1, s35, s1
	v_lshlrev_b64 v[172:173], 12, v[168:169]
	s_lshl_b32 s5, s2, 9
	v_lshlrev_b64 v[176:177], 12, v[196:197]
	v_lshlrev_b64 v[178:179], 12, v[198:199]
	v_lshlrev_b64 v[180:181], 12, v[200:201]
	v_lshlrev_b64 v[182:183], 12, v[202:203]
	v_lshlrev_b64 v[184:185], 12, v[204:205]
	v_lshlrev_b64 v[186:187], 12, v[206:207]
	v_lshlrev_b64 v[188:189], 12, v[208:209]
	v_lshl_add_u64 v[128:129], s[0:1], 0, v[172:173]
	s_and_b32 s8, s5, 0xe00
	s_mov_b32 s9, 0
	v_lshl_add_u64 v[130:131], s[0:1], 0, v[176:177]
	v_lshl_add_u64 v[136:137], s[0:1], 0, v[178:179]
	v_lshl_add_u64 v[138:139], s[0:1], 0, v[180:181]
	v_lshl_add_u64 v[148:149], s[0:1], 0, v[182:183]
	v_lshl_add_u64 v[150:151], s[0:1], 0, v[184:185]
	v_lshl_add_u64 v[156:157], s[0:1], 0, v[186:187]
	v_lshl_add_u64 v[158:159], s[0:1], 0, v[188:189]
	v_lshl_add_u64 v[128:129], v[128:129], 0, s[8:9]
	v_mov_b32_e32 v175, 0
	v_lshlrev_b32_e32 v174, 1, v170
	v_lshl_add_u64 v[130:131], v[130:131], 0, s[8:9]
	v_lshl_add_u64 v[136:137], v[136:137], 0, s[8:9]
	v_lshl_add_u64 v[138:139], v[138:139], 0, s[8:9]
	v_lshl_add_u64 v[148:149], v[148:149], 0, s[8:9]
	v_lshl_add_u64 v[150:151], v[150:151], 0, s[8:9]
	v_lshl_add_u64 v[156:157], v[156:157], 0, s[8:9]
	v_lshl_add_u64 v[158:159], v[158:159], 0, s[8:9]
	v_lshl_add_u64 v[128:129], v[128:129], 0, v[174:175]
	v_lshl_add_u64 v[130:131], v[130:131], 0, v[174:175]
	v_lshl_add_u64 v[136:137], v[136:137], 0, v[174:175]
	v_lshl_add_u64 v[138:139], v[138:139], 0, v[174:175]
	v_lshl_add_u64 v[148:149], v[148:149], 0, v[174:175]
	v_lshl_add_u64 v[150:151], v[150:151], 0, v[174:175]
	v_lshl_add_u64 v[156:157], v[156:157], 0, v[174:175]
	v_lshl_add_u64 v[158:159], v[158:159], 0, v[174:175]
	global_load_dwordx4 v[132:135], v[128:129], off nt
	s_nop 0
	global_load_dwordx4 v[128:131], v[130:131], off nt
	s_nop 0
	global_load_dwordx4 v[140:143], v[136:137], off nt
	s_nop 0
	global_load_dwordx4 v[136:139], v[138:139], off nt
	s_nop 0
	global_load_dwordx4 v[152:155], v[148:149], off nt
	s_nop 0
	global_load_dwordx4 v[148:151], v[150:151], off nt
	s_nop 0
	global_load_dwordx4 v[160:163], v[156:157], off nt
	s_nop 0
	global_load_dwordx4 v[156:159], v[158:159], off nt
	s_cmpk_eq_i32 s34, 0x100
	s_cselect_b64 s[10:11], -1, 0
	s_add_i32 s1, s2, 0x320
	s_cmpk_gt_i32 s2, 0xdf
	s_cselect_b32 s16, s1, 0x420
	v_bfe_u32 v171, v144, 2, 2
	v_lshrrev_b32_e32 v174, 1, v144
	s_mov_b32 s1, 0x7fffff8
	s_movk_i32 s0, 0x220
	v_and_or_b32 v171, v174, s1, v171
	v_lshlrev_b32_e32 v192, 6, v146
	v_lshlrev_b32_e32 v146, 4, v144
	v_mul_lo_u32 v171, v171, s0
	v_lshlrev_b32_e32 v144, 2, v144
	v_lshlrev_b32_e32 v190, 2, v147
	v_lshlrev_b32_e32 v193, 6, v164
	v_lshlrev_b32_e32 v194, 6, v165
	v_lshlrev_b32_e32 v195, 6, v166
	v_mul_lo_u32 v145, v208, s0
	v_mul_lo_u32 v147, v206, s0
	v_mul_lo_u32 v164, v204, s0
	v_mul_lo_u32 v165, v202, s0
	v_mul_lo_u32 v166, v200, s0
	v_mul_lo_u32 v167, v198, s0
	v_mul_lo_u32 v169, v196, s0
	v_mul_lo_u32 v168, v168, s0
	v_add_u32_e32 v196, 0, v171
	v_and_or_b32 v144, v144, 12, s4
	v_add_u32_e32 v145, 0, v145
	v_and_b32_e32 v146, 0x1f0, v146
	v_add_u32_e32 v147, 0, v147
	v_add_u32_e32 v164, 0, v164
	v_add_u32_e32 v165, 0, v165
	v_add_u32_e32 v166, 0, v166
	v_add_u32_e32 v167, 0, v167
	v_add_u32_e32 v169, 0, v169
	v_add_u32_e32 v168, 0, v168
	v_lshlrev_b32_e32 v197, 1, v144
	v_add_u32_e32 v171, 0x4400, v196
	v_add_u32_e32 v207, 0x8800, v196
	v_add_u32_e32 v208, 0xcc00, v196
	s_mov_b32 s5, s9
	v_ashrrev_i32_e32 v191, 31, v190
	v_add_u32_e32 v198, v145, v146
	v_add_u32_e32 v199, v147, v146
	v_add_u32_e32 v200, v164, v146
	v_add_u32_e32 v201, v165, v146
	v_add_u32_e32 v202, v166, v146
	v_add_u32_e32 v203, v167, v146
	v_add_u32_e32 v204, v169, v146
	v_add_u32_e32 v205, v168, v146
	v_lshlrev_b32_e32 v174, 1, v170
	s_mov_b64 s[12:13], 0x3b800800
	s_mov_b32 s17, 0x3b800000
	v_mov_b32_e32 v144, v175
	v_mov_b32_e32 v145, v175
	v_mov_b32_e32 v146, v175
	v_mov_b32_e32 v147, v175
	v_add_u32_e32 v206, v171, v197
	v_add_u32_e32 v207, v207, v197
	v_add_u32_e32 v208, v208, v197
	s_mov_b32 s36, s2
	v_mbcnt_lo_u32_b32 v248, -1, 0
	v_mbcnt_hi_u32_b32 v248, -1, v248
	v_and_b32_e32 v248, 1, v248
	v_cmp_eq_u32_e32 vcc, 1, v248
	v_mov_b32_e32 v246, 0xfffc0010
	v_mov_b32_e32 v247, -1
	v_mov_b32_e32 v250, 16
	v_mov_b32_e32 v251, 0
	v_mov_b32_e32 v252, 0x40010
	v_mov_b32_e32 v253, 0
	v_mov_b32_e32 v254, 16
	v_mov_b32_e32 v255, 0
	s_mov_b64 s[100:101], vcc
	v_cndmask_b32_e32 v246, 0, v246, vcc
	v_cndmask_b32_e32 v247, 0, v247, vcc
	v_mov_b32_e32 v248, 0x40000
	v_cndmask_b32_e32 v250, v248, v250, vcc
	v_cndmask_b32_e32 v252, 0, v252, vcc
	v_mov_b32_e32 v244, 0xfffc0000
	v_cndmask_b32_e32 v254, v244, v254, vcc
	v_cndmask_b32_e32 v255, -1, v255, vcc
	s_branch .LBB0_824

.LBB0_837:
	v_mov_b64_e32 v[166:167], v[146:147]
	v_mov_b64_e32 v[164:165], v[144:145]
	v_add_u32_e32 v209, v196, v197
	ds_read_b64_tr_b16 v[210:211], v209
	ds_read_b64_tr_b16 v[212:213], v209 offset:2176
	v_mov_b64_e32 v[216:217], v[166:167]
	v_mov_b64_e32 v[220:221], v[166:167]
	v_mov_b64_e32 v[224:225], v[166:167]
	v_mov_b64_e32 v[170:171], v[166:167]
	v_mov_b64_e32 v[214:215], v[164:165]
	v_mov_b64_e32 v[218:219], v[164:165]
	v_mov_b64_e32 v[222:223], v[164:165]
	v_mov_b64_e32 v[168:169], v[164:165]
	s_waitcnt lgkmcnt(0)
	v_mfma_f32_16x16x32_bf16 v[214:217], v[210:213], v[0:3], v[214:217]
	v_mfma_f32_16x16x32_bf16 v[218:221], v[210:213], v[16:19], v[218:221]
	v_mfma_f32_16x16x32_bf16 v[222:225], v[210:213], v[32:35], v[222:225]
	v_mfma_f32_16x16x32_bf16 v[168:171], v[210:213], v[48:51], v[168:171]
	ds_read_b64_tr_b16 v[210:211], v206
	ds_read_b64_tr_b16 v[212:213], v206 offset:2176
	s_waitcnt lgkmcnt(0)
	v_mfma_f32_16x16x32_bf16 v[214:217], v[210:213], v[4:7], v[214:217]
	v_mfma_f32_16x16x32_bf16 v[218:221], v[210:213], v[20:23], v[218:221]
	v_mfma_f32_16x16x32_bf16 v[222:225], v[210:213], v[36:39], v[222:225]
	v_mfma_f32_16x16x32_bf16 v[168:171], v[210:213], v[52:55], v[168:171]
	ds_read_b64_tr_b16 v[210:211], v207
	ds_read_b64_tr_b16 v[212:213], v207 offset:2176
	s_waitcnt lgkmcnt(0)
	v_mfma_f32_16x16x32_bf16 v[214:217], v[210:213], v[8:11], v[214:217]
	v_mfma_f32_16x16x32_bf16 v[218:221], v[210:213], v[24:27], v[218:221]
	v_mfma_f32_16x16x32_bf16 v[222:225], v[210:213], v[40:43], v[222:225]
	v_mfma_f32_16x16x32_bf16 v[168:171], v[210:213], v[56:59], v[168:171]
	ds_read_b64_tr_b16 v[210:211], v208
	ds_read_b64_tr_b16 v[212:213], v208 offset:2176
	s_waitcnt lgkmcnt(0)
	v_mfma_f32_16x16x32_bf16 v[214:217], v[210:213], v[12:15], v[214:217]
	v_mfma_f32_16x16x32_bf16 v[218:221], v[210:213], v[28:31], v[218:221]
	v_mfma_f32_16x16x32_bf16 v[222:225], v[210:213], v[44:47], v[222:225]
	v_mfma_f32_16x16x32_bf16 v[168:171], v[210:213], v[60:63], v[168:171]
	ds_read_b64_tr_b16 v[210:211], v209 offset:32
	ds_read_b64_tr_b16 v[212:213], v209 offset:2208
	v_mov_b64_e32 v[228:229], v[166:167]
	v_mov_b64_e32 v[232:233], v[166:167]
	v_mov_b64_e32 v[236:237], v[166:167]
	v_mov_b64_e32 v[226:227], v[164:165]
	v_mov_b64_e32 v[230:231], v[164:165]
	v_mov_b64_e32 v[234:235], v[164:165]
	s_waitcnt lgkmcnt(0)
	v_mfma_f32_16x16x32_bf16 v[226:229], v[210:213], v[0:3], v[226:229]
	v_mfma_f32_16x16x32_bf16 v[230:233], v[210:213], v[16:19], v[230:233]
	v_mfma_f32_16x16x32_bf16 v[234:237], v[210:213], v[32:35], v[234:237]
	v_mfma_f32_16x16x32_bf16 v[164:167], v[210:213], v[48:51], v[164:167]
	ds_read_b64_tr_b16 v[210:211], v206 offset:32
	ds_read_b64_tr_b16 v[212:213], v206 offset:2208
	s_waitcnt lgkmcnt(0)
	v_mfma_f32_16x16x32_bf16 v[226:229], v[210:213], v[4:7], v[226:229]
	v_mfma_f32_16x16x32_bf16 v[230:233], v[210:213], v[20:23], v[230:233]
	v_mfma_f32_16x16x32_bf16 v[234:237], v[210:213], v[36:39], v[234:237]
	v_mfma_f32_16x16x32_bf16 v[164:167], v[210:213], v[52:55], v[164:167]
	ds_read_b64_tr_b16 v[210:211], v207 offset:32
	ds_read_b64_tr_b16 v[212:213], v207 offset:2208
	s_waitcnt lgkmcnt(0)
	v_mfma_f32_16x16x32_bf16 v[226:229], v[210:213], v[8:11], v[226:229]
	v_mfma_f32_16x16x32_bf16 v[230:233], v[210:213], v[24:27], v[230:233]
	v_mfma_f32_16x16x32_bf16 v[234:237], v[210:213], v[40:43], v[234:237]
	v_mfma_f32_16x16x32_bf16 v[164:167], v[210:213], v[56:59], v[164:167]
	ds_read_b64_tr_b16 v[210:211], v208 offset:32
	ds_read_b64_tr_b16 v[212:213], v208 offset:2208
	s_lshl_b32 s14, s38, 12
	s_waitcnt lgkmcnt(0)
	v_mfma_f32_16x16x32_bf16 v[226:229], v[210:213], v[12:15], v[226:229]
	v_mfma_f32_16x16x32_bf16 v[230:233], v[210:213], v[28:31], v[230:233]
	v_mfma_f32_16x16x32_bf16 v[234:237], v[210:213], v[44:47], v[234:237]
	v_mfma_f32_16x16x32_bf16 v[164:167], v[210:213], v[60:63], v[164:167]
	v_add_u32_e32 v210, s37, v192
	v_add_u32_e32 v212, s14, v210
	v_mov_b32_e32 v211, v175
	v_ashrrev_i32_e32 v213, 31, v212
	v_cvt_pk_fp8_f32 v211, v214, v215
	v_mov_b32_e32 v238, v175
	s_lshl_b32 s8, s36, 8
	v_lshlrev_b64 v[212:213], 12, v[212:213]
	v_cvt_pk_fp8_f32 v238, v226, v227
	s_and_b32 s8, s8, 0x700
	v_lshl_add_u64 v[212:213], s[56:57], 0, v[212:213]
	v_lshl_add_u64 v[212:213], v[212:213], 0, s[8:9]
	v_lshl_add_u64 v[212:213], v[212:213], 0, s[4:5]
	v_cvt_pk_fp8_f32 v211, v216, v217 op_sel:[0,0,1]
	v_lshl_add_u64 v[212:213], v[212:213], 0, v[190:191]
	v_cvt_pk_fp8_f32 v238, v228, v229 op_sel:[0,0,1]
	v_lshl_add_u64 v[214:215], v[212:213], 0, s[12:13]
	v_add_co_u32_e32 v212, vcc, s17, v212
	s_nop 15
	s_nop 15
	v_mov_b32_e32 v216, v175
	s_nop 0
	v_addc_co_u32_e32 v213, vcc, 0, v213, vcc
	s_nop 1
	v_mov_b32_dpp v244, v211 quad_perm:[1,0,3,2] row_mask:0xf bank_mask:0xf
	v_mov_b32_dpp v245, v238 quad_perm:[1,0,3,2] row_mask:0xf bank_mask:0xf
	v_lshl_add_u64 v[242:243], v[214:215], 0, v[250:251]
	v_lshl_add_u64 v[212:213], v[214:215], 0, v[246:247]
	v_cndmask_b32_e64 v245, v211, v245, s[100:101]
	v_cndmask_b32_e64 v244, v244, v238, s[100:101]
	global_store_dword v[212:213], v245, off
	global_store_dword v[242:243], v244, off
	v_add_u32_e32 v211, s37, v193
	v_add_u32_e32 v212, s14, v211
	v_ashrrev_i32_e32 v213, 31, v212
	v_cvt_pk_fp8_f32 v216, v218, v219
	v_mov_b32_e32 v217, v175
	v_lshlrev_b64 v[212:213], 12, v[212:213]
	v_cvt_pk_fp8_f32 v217, v230, v231
	v_lshl_add_u64 v[212:213], s[56:57], 0, v[212:213]
	v_lshl_add_u64 v[212:213], v[212:213], 0, s[8:9]
	v_lshl_add_u64 v[212:213], v[212:213], 0, s[4:5]
	v_cvt_pk_fp8_f32 v216, v220, v221 op_sel:[0,0,1]
	v_lshl_add_u64 v[212:213], v[212:213], 0, v[190:191]
	v_cvt_pk_fp8_f32 v217, v232, v233 op_sel:[0,0,1]
	v_lshl_add_u64 v[214:215], v[212:213], 0, s[12:13]
	v_add_co_u32_e32 v212, vcc, s17, v212
	v_mov_b32_e32 v218, v175
	s_nop 0
	v_addc_co_u32_e32 v213, vcc, 0, v213, vcc
	s_nop 1
	v_mov_b32_dpp v244, v216 quad_perm:[1,0,3,2] row_mask:0xf bank_mask:0xf
	v_mov_b32_dpp v245, v217 quad_perm:[1,0,3,2] row_mask:0xf bank_mask:0xf
	v_lshl_add_u64 v[242:243], v[214:215], 0, v[250:251]
	v_lshl_add_u64 v[212:213], v[214:215], 0, v[246:247]
	v_cndmask_b32_e64 v245, v216, v245, s[100:101]
	v_cndmask_b32_e64 v244, v244, v217, s[100:101]
	global_store_dword v[212:213], v245, off
	global_store_dword v[242:243], v244, off
	v_add_u32_e32 v212, s37, v194
	v_add_u32_e32 v214, s14, v212
	v_mov_b32_e32 v213, v175
	v_ashrrev_i32_e32 v215, 31, v214
	v_cvt_pk_fp8_f32 v213, v222, v223
	v_lshlrev_b64 v[214:215], 12, v[214:215]
	v_cvt_pk_fp8_f32 v218, v234, v235
	v_lshl_add_u64 v[214:215], s[56:57], 0, v[214:215]
	v_lshl_add_u64 v[214:215], v[214:215], 0, s[8:9]
	v_lshl_add_u64 v[214:215], v[214:215], 0, s[4:5]
	v_cvt_pk_fp8_f32 v213, v224, v225 op_sel:[0,0,1]
	v_lshl_add_u64 v[214:215], v[214:215], 0, v[190:191]
	v_cvt_pk_fp8_f32 v218, v236, v237 op_sel:[0,0,1]
	v_lshl_add_u64 v[216:217], v[214:215], 0, s[12:13]
	v_add_co_u32_e32 v214, vcc, s17, v214
	s_and_b32 s15, s37, 0xffffffdf
	s_nop 0
	v_addc_co_u32_e32 v215, vcc, 0, v215, vcc
	s_nop 1
	v_mov_b32_dpp v244, v213 quad_perm:[1,0,3,2] row_mask:0xf bank_mask:0xf
	v_mov_b32_dpp v245, v218 quad_perm:[1,0,3,2] row_mask:0xf bank_mask:0xf
	v_lshl_add_u64 v[242:243], v[216:217], 0, v[250:251]
	v_lshl_add_u64 v[214:215], v[216:217], 0, v[246:247]
	v_cndmask_b32_e64 v245, v213, v245, s[100:101]
	v_cndmask_b32_e64 v244, v244, v218, s[100:101]
	global_store_dword v[214:215], v245, off
	global_store_dword v[242:243], v244, off
	v_add_u32_e32 v213, s37, v195
	v_add_u32_e32 v214, s14, v213
	v_mov_b32_e32 v216, v175
	v_ashrrev_i32_e32 v215, 31, v214
	v_cvt_pk_fp8_f32 v216, v168, v169
	v_mov_b32_e32 v217, v175
	v_lshlrev_b64 v[214:215], 12, v[214:215]
	v_cvt_pk_fp8_f32 v217, v164, v165
	v_lshl_add_u64 v[214:215], s[56:57], 0, v[214:215]
	v_lshl_add_u64 v[214:215], v[214:215], 0, s[8:9]
	v_lshl_add_u64 v[214:215], v[214:215], 0, s[4:5]
	v_cvt_pk_fp8_f32 v216, v170, v171 op_sel:[0,0,1]
	v_lshl_add_u64 v[214:215], v[214:215], 0, v[190:191]
	v_cvt_pk_fp8_f32 v217, v166, v167 op_sel:[0,0,1]
	v_add_co_u32_e32 v164, vcc, 0x3b800000, v214
	s_cmp_eq_u32 s15, 0
	s_nop 0
	v_addc_co_u32_e32 v165, vcc, 0, v215, vcc
	v_lshl_add_u64 v[168:169], v[214:215], 0, s[12:13]
	s_nop 1
	v_mov_b32_dpp v244, v216 quad_perm:[1,0,3,2] row_mask:0xf bank_mask:0xf
	v_mov_b32_dpp v245, v217 quad_perm:[1,0,3,2] row_mask:0xf bank_mask:0xf
	v_lshl_add_u64 v[242:243], v[168:169], 0, v[250:251]
	v_lshl_add_u64 v[164:165], v[168:169], 0, v[246:247]
	v_cndmask_b32_e64 v245, v216, v245, s[100:101]
	v_cndmask_b32_e64 v244, v244, v217, s[100:101]
	global_store_dword v[164:165], v245, off
	global_store_dword v[242:243], v244, off
	s_cbranch_scc1 .LBB0_839
	v_mov_b64_e32 v[166:167], v[146:147]
	v_mov_b64_e32 v[164:165], v[144:145]
	ds_read_b64_tr_b16 v[214:215], v209
	ds_read_b64_tr_b16 v[216:217], v209 offset:2176
	v_mov_b64_e32 v[220:221], v[166:167]
	v_mov_b64_e32 v[224:225], v[166:167]
	v_mov_b64_e32 v[228:229], v[166:167]
	v_mov_b64_e32 v[170:171], v[166:167]
	v_mov_b64_e32 v[218:219], v[164:165]
	v_mov_b64_e32 v[222:223], v[164:165]
	v_mov_b64_e32 v[226:227], v[164:165]
	v_mov_b64_e32 v[168:169], v[164:165]
	s_waitcnt lgkmcnt(0)
	v_mfma_f32_16x16x32_bf16 v[218:221], v[214:217], v[64:67], v[218:221]
	v_mfma_f32_16x16x32_bf16 v[222:225], v[214:217], v[80:83], v[222:225]
	v_mfma_f32_16x16x32_bf16 v[226:229], v[214:217], v[96:99], v[226:229]
	v_mfma_f32_16x16x32_bf16 v[168:171], v[214:217], v[112:115], v[168:171]
	ds_read_b64_tr_b16 v[214:215], v206
	ds_read_b64_tr_b16 v[216:217], v206 offset:2176
	s_waitcnt lgkmcnt(0)
	v_mfma_f32_16x16x32_bf16 v[218:221], v[214:217], v[68:71], v[218:221]
	v_mfma_f32_16x16x32_bf16 v[222:225], v[214:217], v[84:87], v[222:225]
	v_mfma_f32_16x16x32_bf16 v[226:229], v[214:217], v[100:103], v[226:229]
	v_mfma_f32_16x16x32_bf16 v[168:171], v[214:217], v[116:119], v[168:171]
	ds_read_b64_tr_b16 v[214:215], v207
	ds_read_b64_tr_b16 v[216:217], v207 offset:2176
	s_waitcnt lgkmcnt(0)
	v_mfma_f32_16x16x32_bf16 v[218:221], v[214:217], v[72:75], v[218:221]
	v_mfma_f32_16x16x32_bf16 v[222:225], v[214:217], v[88:91], v[222:225]
	v_mfma_f32_16x16x32_bf16 v[226:229], v[214:217], v[104:107], v[226:229]
	v_mfma_f32_16x16x32_bf16 v[168:171], v[214:217], v[120:123], v[168:171]
	ds_read_b64_tr_b16 v[214:215], v208
	ds_read_b64_tr_b16 v[216:217], v208 offset:2176
	s_waitcnt lgkmcnt(0)
	v_mfma_f32_16x16x32_bf16 v[218:221], v[214:217], v[76:79], v[218:221]
	v_mfma_f32_16x16x32_bf16 v[222:225], v[214:217], v[92:95], v[222:225]
	v_mfma_f32_16x16x32_bf16 v[226:229], v[214:217], v[108:111], v[226:229]
	v_mfma_f32_16x16x32_bf16 v[168:171], v[214:217], v[124:127], v[168:171]
	ds_read_b64_tr_b16 v[214:215], v209 offset:32
	ds_read_b64_tr_b16 v[216:217], v209 offset:2208
	v_mov_b64_e32 v[232:233], v[166:167]
	v_mov_b64_e32 v[236:237], v[166:167]
	v_mov_b64_e32 v[240:241], v[166:167]
	v_mov_b64_e32 v[230:231], v[164:165]
	v_mov_b64_e32 v[234:235], v[164:165]
	v_mov_b64_e32 v[238:239], v[164:165]
	s_waitcnt lgkmcnt(0)
	v_mfma_f32_16x16x32_bf16 v[230:233], v[214:217], v[64:67], v[230:233]
	v_mfma_f32_16x16x32_bf16 v[234:237], v[214:217], v[80:83], v[234:237]
	v_mfma_f32_16x16x32_bf16 v[238:241], v[214:217], v[96:99], v[238:241]
	v_mfma_f32_16x16x32_bf16 v[164:167], v[214:217], v[112:115], v[164:167]
	ds_read_b64_tr_b16 v[214:215], v206 offset:32
	ds_read_b64_tr_b16 v[216:217], v206 offset:2208
	s_waitcnt lgkmcnt(0)
	v_mfma_f32_16x16x32_bf16 v[230:233], v[214:217], v[68:71], v[230:233]
	v_mfma_f32_16x16x32_bf16 v[234:237], v[214:217], v[84:87], v[234:237]
	v_mfma_f32_16x16x32_bf16 v[238:241], v[214:217], v[100:103], v[238:241]
	v_mfma_f32_16x16x32_bf16 v[164:167], v[214:217], v[116:119], v[164:167]
	ds_read_b64_tr_b16 v[214:215], v207 offset:32
	ds_read_b64_tr_b16 v[216:217], v207 offset:2208
	s_waitcnt lgkmcnt(0)
	v_mfma_f32_16x16x32_bf16 v[230:233], v[214:217], v[72:75], v[230:233]
	v_mfma_f32_16x16x32_bf16 v[234:237], v[214:217], v[88:91], v[234:237]
	v_mfma_f32_16x16x32_bf16 v[238:241], v[214:217], v[104:107], v[238:241]
	v_mfma_f32_16x16x32_bf16 v[164:167], v[214:217], v[120:123], v[164:167]
	ds_read_b64_tr_b16 v[214:215], v208 offset:32
	ds_read_b64_tr_b16 v[216:217], v208 offset:2208
	v_sub_u32_e32 v209, s14, v210
	s_waitcnt lgkmcnt(0)
	v_mfma_f32_16x16x32_bf16 v[230:233], v[214:217], v[76:79], v[230:233]
	v_mfma_f32_16x16x32_bf16 v[234:237], v[214:217], v[92:95], v[234:237]
	v_mfma_f32_16x16x32_bf16 v[238:241], v[214:217], v[108:111], v[238:241]
	v_mfma_f32_16x16x32_bf16 v[164:167], v[214:217], v[124:127], v[164:167]
	v_add_u32_e32 v214, 0x1000, v209
	v_mov_b32_e32 v209, v175
	v_ashrrev_i32_e32 v215, 31, v214
	v_cvt_pk_fp8_f32 v209, v218, v219
	v_mov_b32_e32 v210, v175
	v_lshlrev_b64 v[214:215], 12, v[214:215]
	v_cvt_pk_fp8_f32 v210, v230, v231
	v_lshl_add_u64 v[214:215], s[56:57], 0, v[214:215]
	v_lshl_add_u64 v[214:215], v[214:215], 0, s[8:9]
	v_lshl_add_u64 v[214:215], v[214:215], 0, s[4:5]
	v_cvt_pk_fp8_f32 v209, v220, v221 op_sel:[0,0,1]
	v_lshl_add_u64 v[214:215], v[214:215], 0, v[190:191]
	v_cvt_pk_fp8_f32 v210, v232, v233 op_sel:[0,0,1]
	v_lshl_add_u64 v[216:217], v[214:215], 0, s[12:13]
	v_add_co_u32_e32 v214, vcc, s17, v214
	s_nop 15
	s_nop 15
	s_nop 1
	v_addc_co_u32_e32 v215, vcc, 0, v215, vcc
	s_nop 1
	v_mov_b32_dpp v244, v209 quad_perm:[1,0,3,2] row_mask:0xf bank_mask:0xf
	v_mov_b32_dpp v245, v210 quad_perm:[1,0,3,2] row_mask:0xf bank_mask:0xf
	v_lshl_add_u64 v[242:243], v[216:217], 0, v[254:255]
	v_lshl_add_u64 v[214:215], v[216:217], 0, v[252:253]
	v_cndmask_b32_e64 v245, v209, v245, s[100:101]
	v_cndmask_b32_e64 v244, v244, v210, s[100:101]
	global_store_dword v[214:215], v245, off
	global_store_dword v[242:243], v244, off
	v_sub_u32_e32 v209, s14, v211
	v_add_u32_e32 v210, 0x1000, v209
	v_mov_b32_e32 v209, v175
	v_ashrrev_i32_e32 v211, 31, v210
	v_cvt_pk_fp8_f32 v209, v222, v223
	v_mov_b32_e32 v216, v175
	v_lshlrev_b64 v[210:211], 12, v[210:211]
	v_cvt_pk_fp8_f32 v216, v234, v235
	v_lshl_add_u64 v[210:211], s[56:57], 0, v[210:211]
	v_lshl_add_u64 v[210:211], v[210:211], 0, s[8:9]
	v_lshl_add_u64 v[210:211], v[210:211], 0, s[4:5]
	v_cvt_pk_fp8_f32 v209, v224, v225 op_sel:[0,0,1]
	v_lshl_add_u64 v[210:211], v[210:211], 0, v[190:191]
	v_cvt_pk_fp8_f32 v216, v236, v237 op_sel:[0,0,1]
	v_lshl_add_u64 v[214:215], v[210:211], 0, s[12:13]
	v_add_co_u32_e32 v210, vcc, s17, v210
	s_nop 1
	v_addc_co_u32_e32 v211, vcc, 0, v211, vcc
	s_nop 1
	v_mov_b32_dpp v244, v209 quad_perm:[1,0,3,2] row_mask:0xf bank_mask:0xf
	v_mov_b32_dpp v245, v216 quad_perm:[1,0,3,2] row_mask:0xf bank_mask:0xf
	v_lshl_add_u64 v[242:243], v[214:215], 0, v[254:255]
	v_lshl_add_u64 v[210:211], v[214:215], 0, v[252:253]
	v_cndmask_b32_e64 v245, v209, v245, s[100:101]
	v_cndmask_b32_e64 v244, v244, v216, s[100:101]
	global_store_dword v[210:211], v245, off
	global_store_dword v[242:243], v244, off
	v_sub_u32_e32 v209, s14, v212
	v_add_u32_e32 v210, 0x1000, v209
	v_mov_b32_e32 v209, v175
	v_ashrrev_i32_e32 v211, 31, v210
	v_cvt_pk_fp8_f32 v209, v226, v227
	v_mov_b32_e32 v212, v175
	v_lshlrev_b64 v[210:211], 12, v[210:211]
	v_cvt_pk_fp8_f32 v212, v238, v239
	v_lshl_add_u64 v[210:211], s[56:57], 0, v[210:211]
	v_lshl_add_u64 v[210:211], v[210:211], 0, s[8:9]
	v_lshl_add_u64 v[210:211], v[210:211], 0, s[4:5]
	v_cvt_pk_fp8_f32 v209, v228, v229 op_sel:[0,0,1]
	v_lshl_add_u64 v[210:211], v[210:211], 0, v[190:191]
	v_cvt_pk_fp8_f32 v212, v240, v241 op_sel:[0,0,1]
	v_lshl_add_u64 v[214:215], v[210:211], 0, s[12:13]
	v_add_co_u32_e32 v210, vcc, s17, v210
	s_nop 1
	v_addc_co_u32_e32 v211, vcc, 0, v211, vcc
	s_nop 1
	v_mov_b32_dpp v244, v209 quad_perm:[1,0,3,2] row_mask:0xf bank_mask:0xf
	v_mov_b32_dpp v245, v212 quad_perm:[1,0,3,2] row_mask:0xf bank_mask:0xf
	v_lshl_add_u64 v[242:243], v[214:215], 0, v[254:255]
	v_lshl_add_u64 v[210:211], v[214:215], 0, v[252:253]
	v_cndmask_b32_e64 v245, v209, v245, s[100:101]
	v_cndmask_b32_e64 v244, v244, v212, s[100:101]
	global_store_dword v[210:211], v245, off
	global_store_dword v[242:243], v244, off
	v_sub_u32_e32 v209, s14, v213
	v_add_u32_e32 v210, 0x1000, v209
	v_mov_b32_e32 v209, v175
	v_ashrrev_i32_e32 v211, 31, v210
	v_cvt_pk_fp8_f32 v209, v168, v169
	v_mov_b32_e32 v212, v175
	v_lshlrev_b64 v[210:211], 12, v[210:211]
	v_cvt_pk_fp8_f32 v212, v164, v165
	v_lshl_add_u64 v[210:211], s[56:57], 0, v[210:211]
	v_lshl_add_u64 v[210:211], v[210:211], 0, s[8:9]
	v_lshl_add_u64 v[210:211], v[210:211], 0, s[4:5]
	v_cvt_pk_fp8_f32 v209, v170, v171 op_sel:[0,0,1]
	v_lshl_add_u64 v[210:211], v[210:211], 0, v[190:191]
	v_cvt_pk_fp8_f32 v212, v166, v167 op_sel:[0,0,1]
	v_add_co_u32_e32 v164, vcc, 0x3b800000, v210
	v_lshl_add_u64 v[168:169], v[210:211], 0, s[12:13]
	s_nop 0
	v_addc_co_u32_e32 v165, vcc, 0, v211, vcc
	s_nop 1
	v_mov_b32_dpp v244, v209 quad_perm:[1,0,3,2] row_mask:0xf bank_mask:0xf
	v_mov_b32_dpp v245, v212 quad_perm:[1,0,3,2] row_mask:0xf bank_mask:0xf
	v_lshl_add_u64 v[242:243], v[168:169], 0, v[254:255]
	v_lshl_add_u64 v[164:165], v[168:169], 0, v[252:253]
	v_cndmask_b32_e64 v245, v209, v245, s[100:101]
	v_cndmask_b32_e64 v244, v244, v212, s[100:101]
	global_store_dword v[164:165], v245, off
	global_store_dword v[242:243], v244, off

.LBB0_877:
	s_andn2_saveexec_b64 s[4:5], s[4:5]
	s_cbranch_execz .LBB0_895
.LBB0_895:
	s_or_b64 exec, exec, s[0:1]
	s_waitcnt lgkmcnt(0)
	s_barrier

.LBB0_1027:
	s_andn2_saveexec_b64 s[4:5], s[4:5]
	s_cbranch_execz .LBB0_1045
.LBB0_1045:
	s_or_b64 exec, exec, s[0:1]
	s_waitcnt lgkmcnt(0)
	s_barrier

.LBB0_1153:
	s_andn2_saveexec_b64 s[4:5], s[4:5]
	s_cbranch_execz .LBB0_1171
.LBB0_1171:
	s_or_b64 exec, exec, s[0:1]
	s_waitcnt lgkmcnt(0)
	s_barrier

.LBB0_1272:
	s_andn2_saveexec_b64 s[4:5], s[4:5]
	s_cbranch_execz .LBB0_1290
.LBB0_1290:
	s_or_b64 exec, exec, s[0:1]
	s_waitcnt lgkmcnt(0)
	s_barrier

.LBB0_1398:
	s_or_b64 exec, exec, s[10:11]
	v_cvt_f32_u32_e32 v4, v2
	s_waitcnt vmcnt(0)
	v_readfirstlane_b32 s10, v3
	v_sub_u32_e32 v3, 0, v2
	v_rcp_iflag_f32_e32 v4, v4
	v_add_u32_e32 v5, s10, v1
	v_mul_f32_e32 v4, 0x4f7ffffe, v4
	v_cvt_u32_f32_e32 v4, v4
	v_mul_lo_u32 v1, v3, v4
	v_mul_hi_u32 v1, v4, v1
	v_add_u32_e32 v1, v4, v1
	v_mul_hi_u32 v1, v5, v1
	v_mul_lo_u32 v3, v1, v2
	v_sub_u32_e32 v3, v5, v3
	v_add_u32_e32 v4, 1, v1
	v_cmp_ge_u32_e32 vcc, v3, v2
	s_nop 1
	v_cndmask_b32_e32 v1, v1, v4, vcc
	v_sub_u32_e32 v4, v3, v2
	v_cndmask_b32_e32 v3, v3, v4, vcc
	v_add_u32_e32 v4, 1, v1
	v_cmp_ge_u32_e32 vcc, v3, v2
	v_add_u32_e32 v3, 1, v5
	s_nop 0
	v_cndmask_b32_e32 v1, v1, v4, vcc
	v_mul_lo_u32 v4, v2, v1
	v_add_u32_e32 v2, v4, v2
	v_add_u32_e32 v252, 1, v1
	v_mul_lo_u32 v252, v252, v0
	v_cmp_ne_u32_e32 vcc, v3, v2
	s_cbranch_vccnz .Lxb_nl_10
	buffer_wbl2 sc1
	s_waitcnt vmcnt(0) lgkmcnt(0)
	v_mov_b32_e32 v253, 0x3500
	v_mov_b32_e32 v254, 1
	global_atomic_add v253, v254, s[56:57]
	s_mov_b64 vcc, exec
.Lxb_nl_10:
	s_and_saveexec_b64 s[10:11], vcc
	s_xor_b64 s[10:11], exec, s[10:11]
	s_cbranch_execz .LBB0_1412
	s_waitcnt lgkmcnt(0)
	v_cmp_eq_u32_e32 vcc, v5, v4
	s_cbranch_vccz .Lxb_nf_10
	buffer_wbl2 sc1
.Lxb_nf_10:
	v_mov_b32_e32 v0, 0x3000
	global_load_dword v0, v0, s[56:57] offset:1280 sc1
	s_add_u32 s24, s56, 0x3500
	s_addc_u32 s25, s57, 0
	s_waitcnt vmcnt(0)
	v_cmp_lt_u32_e32 vcc, v0, v252
	s_and_saveexec_b64 s[12:13], vcc
	s_cbranch_execz .LBB0_1411
	s_mov_b32 s33, 1
	s_mov_b64 s[26:27], 0
	v_mov_b32_e32 v0, 0
	s_branch .LBB0_1402

.LBB0_1406:
	global_load_dword v2, v0, s[24:25] sc1
	s_add_i32 s33, s33, 1
	s_mov_b64 s[38:39], -1
	s_waitcnt vmcnt(0)
	v_cmp_ge_u32_e32 vcc, v2, v252
	s_orn2_b64 s[36:37], vcc, exec
	s_branch .LBB0_1401

.LBB0_1412:
	s_andn2_saveexec_b64 s[10:11], s[10:11]
	s_cbranch_execz .LBB0_1430
.LBB0_1430:
	s_or_b64 exec, exec, s[0:1]
	s_waitcnt lgkmcnt(0)
	v_mov_b64_e32 v[0:1], s[2:3]
	s_barrier
	v_mbcnt_lo_u32_b32 v2, -1, 0
	v_mbcnt_hi_u32_b32 v2, -1, v2
	s_lshl_b32 s12, s35, 4
	v_mad_i64_i32 v[0:1], s[0:1], v2, s34, v[0:1]
	s_mov_b32 s13, 0
	v_cmp_gt_i64_e32 vcc, s[12:13], v[0:1]
	v_mov_b32_e32 v64, 0
	v_mov_b32_e32 v234, -1
	v_mov_b32_e32 v65, 0
	v_mov_b32_e32 v66, 0
	v_mov_b32_e32 v67, 0
	s_and_saveexec_b64 s[0:1], vcc
	s_cbranch_execz .LBB0_1432
	v_ashrrev_i32_e32 v1, 31, v0
	v_lshrrev_b32_e32 v1, 29, v1
	v_add_u32_e32 v1, v0, v1
	v_ashrrev_i32_e32 v2, 3, v1
	v_and_b32_e32 v1, -8, v1
	v_sub_u32_e32 v0, v0, v1
	v_alignbit_b32 v1, s35, v0, 31
	v_mul_lo_u32 v0, v1, v0
	v_add_u32_e32 v0, v0, v2
	v_ashrrev_i32_e32 v1, 31, v0
	v_lshrrev_b32_e32 v1, 25, v1
	v_add_u32_e32 v1, v0, v1
	v_ashrrev_i32_e32 v2, 7, v1
	v_lshlrev_b32_e32 v2, 3, v2
	v_sub_u32_e32 v3, s35, v2
	v_min_i32_e32 v3, 8, v3
	v_sub_u32_e32 v4, 0, v3
	v_max_i32_e32 v4, v3, v4
	v_cvt_f32_u32_e32 v5, v4
	v_and_b32_e32 v1, 0xffffff80, v1
	v_sub_u32_e32 v7, 0, v4
	v_sub_u32_e32 v0, v0, v1
	v_rcp_iflag_f32_e32 v5, v5
	v_sub_u32_e32 v1, 0, v0
	v_max_i32_e32 v1, v0, v1
	v_xor_b32_e32 v6, v0, v3
	v_mul_f32_e32 v5, 0x4f7ffffe, v5
	v_cvt_u32_f32_e32 v5, v5
	v_ashrrev_i32_e32 v6, 31, v6
	s_movk_i32 s10, 0x100
	v_mul_lo_u32 v7, v7, v5
	v_mul_hi_u32 v7, v5, v7
	v_add_u32_e32 v5, v5, v7
	v_mul_hi_u32 v5, v1, v5
	v_mul_lo_u32 v7, v5, v4
	v_sub_u32_e32 v1, v1, v7
	s_waitcnt vmcnt(2)
	v_add_u32_e32 v8, 1, v5
	v_cmp_ge_u32_e32 vcc, v1, v4
	v_sub_u32_e32 v7, v1, v4
	s_nop 0
	v_cndmask_b32_e32 v5, v5, v8, vcc
	v_cndmask_b32_e32 v1, v1, v7, vcc
	v_add_u32_e32 v7, 1, v5
	v_cmp_ge_u32_e32 vcc, v1, v4
	s_nop 1
	v_cndmask_b32_e32 v1, v5, v7, vcc
	v_xor_b32_e32 v1, v1, v6
	v_sub_u32_e32 v1, v1, v6
	v_mul_lo_u32 v3, v1, v3
	v_sub_u32_e32 v0, v0, v3
	v_add3_u32 v0, v2, v0, s10
	v_lshl_add_u32 v2, v0, 4, 0
	v_add_u32_e32 v2, 0x21010, v2
	ds_read_b128 v[64:67], v2
	v_lshl_or_b32 v234, v1, 16, v0

.LBB0_1495:
	s_andn2_saveexec_b64 s[4:5], s[4:5]
	s_cbranch_execz .LBB0_1513
.LBB0_1513:
	s_or_b64 exec, exec, s[0:1]
	s_waitcnt lgkmcnt(0)
	s_barrier

	.amdhsa_kernel _Z6mk_fwd6Params
		.amdhsa_group_segment_fixed_size 0
		.amdhsa_private_segment_fixed_size 0
		.amdhsa_kernarg_size 416
		.amdhsa_user_sgpr_count 2
		.amdhsa_user_sgpr_dispatch_ptr 0
		.amdhsa_user_sgpr_queue_ptr 0
		.amdhsa_user_sgpr_kernarg_segment_ptr 1
		.amdhsa_user_sgpr_dispatch_id 0
		.amdhsa_user_sgpr_kernarg_preload_length 0
		.amdhsa_user_sgpr_kernarg_preload_offset 0
		.amdhsa_user_sgpr_private_segment_size 0
		.amdhsa_uses_dynamic_stack 0
		.amdhsa_enable_private_segment 0
		.amdhsa_system_sgpr_workgroup_id_x 1
		.amdhsa_system_sgpr_workgroup_id_y 0
		.amdhsa_system_sgpr_workgroup_id_z 0
		.amdhsa_system_sgpr_workgroup_info 0
		.amdhsa_system_vgpr_workitem_id 0
		.amdhsa_next_free_vgpr 256
		.amdhsa_next_free_sgpr 102
		.amdhsa_accum_offset 256
		.amdhsa_reserve_vcc 1
		.amdhsa_float_round_mode_32 0
		.amdhsa_float_round_mode_16_64 0
		.amdhsa_float_denorm_mode_32 3
		.amdhsa_float_denorm_mode_16_64 3
		.amdhsa_dx10_clamp 1
		.amdhsa_ieee_mode 1
		.amdhsa_fp16_overflow 0
		.amdhsa_tg_split 0
		.amdhsa_exception_fp_ieee_invalid_op 0
		.amdhsa_exception_fp_denorm_src 0
		.amdhsa_exception_fp_ieee_div_zero 0
		.amdhsa_exception_fp_ieee_overflow 0
		.amdhsa_exception_fp_ieee_underflow 0
		.amdhsa_exception_fp_ieee_inexact 0
		.amdhsa_exception_int_div_zero 0
	.end_amdhsa_kernel

amdhsa.kernels:
  - .agpr_count:     0
    .args:
      - .offset:         0
        .size:           160
        .value_kind:     by_value
      - .offset:         160
        .size:           4
        .value_kind:     hidden_block_count_x
      - .offset:         164
        .size:           4
        .value_kind:     hidden_block_count_y
      - .offset:         168
        .size:           4
        .value_kind:     hidden_block_count_z
      - .offset:         172
        .size:           2
        .value_kind:     hidden_group_size_x
      - .offset:         174
        .size:           2
        .value_kind:     hidden_group_size_y
      - .offset:         176
        .size:           2
        .value_kind:     hidden_group_size_z
      - .offset:         178
        .size:           2
        .value_kind:     hidden_remainder_x
      - .offset:         180
        .size:           2
        .value_kind:     hidden_remainder_y
      - .offset:         182
        .size:           2
        .value_kind:     hidden_remainder_z
      - .offset:         200
        .size:           8
        .value_kind:     hidden_global_offset_x
      - .offset:         208
        .size:           8
        .value_kind:     hidden_global_offset_y
      - .offset:         216
        .size:           8
        .value_kind:     hidden_global_offset_z
      - .offset:         224
        .size:           2
        .value_kind:     hidden_grid_dims
      - .offset:         280
        .size:           4
        .value_kind:     hidden_dynamic_lds_size
    .group_segment_fixed_size: 0
    .kernarg_segment_align: 8
    .kernarg_segment_size: 416
    .language:       OpenCL C
    .language_version:
      - 2
      - 0
    .max_flat_workgroup_size: 512
    .name:           _Z6mk_fwd6Params
    .private_segment_fixed_size: 0
    .sgpr_count:     108
    .sgpr_spill_count: 14
    .symbol:         _Z6mk_fwd6Params.kd
    .uniform_work_group_size: 1
    .uses_dynamic_stack: false
    .vgpr_count:     256
    .vgpr_spill_count: 0
    .wavefront_size: 64
